# attention loop: staging global loads of the next K/V tile issued at the top of each half (before the QK^T+softmax block) instead of just before P.V, on top of the VALU/MFMA interleave
# baseline (speedup 1.0000x reference)
; #define LAS __attribute__((address_space(3)))
; #define SBAR() __builtin_amdgcn_sched_barrier(0)
; #define SLOAD(k0) do { sr_.vs0 = *reinterpret_cast<const bf16x8*>(&Vh[(long)((k0) + vr) * DVV + vc]); \
;     sr_.ks0 = *reinterpret_cast<const bf16x8*>(&Kh[(long)((k0) + sr) * KROW + sc]); sr_.ks1 = *reinterpret_cast<const bf16x8*>(&Kh[(long)((k0) + 32 + sr) * KROW + sc]); } while (0)
; __device__ __forceinline__ void qkt(f32x16& p0, f32x16& p1, const LAS char* Ks, const bf16x8* qr, int r32, int hi, float nm) {
; #pragma unroll
;   for (int r = 0; r < 16; ++r) { p0[r] = nm; p1[r] = nm; }
; #pragma unroll
;   for (int d0 = 0; d0 < DQK / 16; ++d0) { int cb = (d0 * 16 + hi * 8) * 2;
;     bf16x8 b0 = *reinterpret_cast<const LAS bf16x8*>(Ks + KSWZ(r32, cb));
;     bf16x8 b1 = *reinterpret_cast<const LAS bf16x8*>(Ks + KSWZ(32 + r32, cb));
;     __builtin_amdgcn_s_setprio(1);
;     p0 = __builtin_amdgcn_mfma_f32_32x32x16_bf16(b0, qr[d0], p0, 0, 0, 0);
;     p1 = __builtin_amdgcn_mfma_f32_32x32x16_bf16(b1, qr[d0], p1, 0, 0, 0);
;     __builtin_amdgcn_s_setprio(0); }
; }
; __device__ __forceinline__ void attn_body(const bf16_t* __restrict__ Qb, const bf16_t* __restrict__ Kh, const bf16_t* __restrict__ Vh, unsigned char* __restrict__ Ob, int ldo, int seq, LAS char* lds, const int wv, const float kbound, const float oscale) {
;     ...
;     SBAR(); qkt(pB0, pB1, K_lds + b1 * SHM_K, qr, r32, hi, nm);
;     finishSM(pA0, pA1, l_reg, pa0, pa1, pa2, pa3); SBAR();
;     if (j + 3 < NT) SLOAD((j + 3) * KVBLK); SBAR();
.LBB0_603:
	s_mov_b32 s72, s4
	s_lshl_b32 s4, s70, 14
	s_add_i32 s73, s4, 0
	v_add_u32_e32 v242, s73, v192
	s_cmp_lt_u32 s71, 61
	s_cselect_b64 s[4:5], -1, 0
	s_cmp_gt_u32 s71, 60
	v_lshl_add_u64 v[180:181], s[22:23], 0, v[176:177]
	v_lshl_add_u64 v[178:179], s[22:23], 0, v[174:175]
	s_cbranch_scc1 .LBB0_605
	s_waitcnt lgkmcnt(0)
	v_add_co_u32_e32 v46, vcc, 0x66006000, v180
	s_nop 1
	v_addc_co_u32_e32 v47, vcc, 0, v181, vcc
	s_waitcnt vmcnt(1)
	v_add_co_u32_e32 v156, vcc, 0x6200c000, v178
	s_nop 1
	v_addc_co_u32_e32 v157, vcc, 0, v179, vcc
	global_load_dwordx4 v[152:155], v[46:47], off
	s_nop 0
	global_load_dwordx4 v[156:159], v[156:157], off
	v_add_co_u32_e32 v46, vcc, 0x6200e000, v178
	s_nop 1
	v_addc_co_u32_e32 v47, vcc, 0, v179, vcc
	global_load_dwordx4 v[160:163], v[46:47], off
; #define SBAR() __builtin_amdgcn_sched_barrier(0)
; #define SLOAD(k0) do { sr_.vs0 = *reinterpret_cast<const bf16x8*>(&Vh[(long)((k0) + vr) * DVV + vc]); \
;     sr_.ks0 = *reinterpret_cast<const bf16x8*>(&Kh[(long)((k0) + sr) * KROW + sc]); sr_.ks1 = *reinterpret_cast<const bf16x8*>(&Kh[(long)((k0) + 32 + sr) * KROW + sc]); } while (0)
; template <int D0> __device__ __forceinline__ void pv_one(f32x16& od, int vb, bf16x8 pa0, bf16x8 pa1, bf16x8 pa2, bf16x8 pa3) {
;   const s16x4 l0 = tr_read<v_rd_off(D0, 0, 0)>(vb), h0 = tr_read<v_rd_off(D0, 0, 1)>(vb), l1 = tr_read<v_rd_off(D0, 1, 0)>(vb), h1 = tr_read<v_rd_off(D0, 1, 1)>(vb);
;   const s16x4 l2 = tr_read<v_rd_off(D0, 2, 0)>(vb), h2 = tr_read<v_rd_off(D0, 2, 1)>(vb), l3 = tr_read<v_rd_off(D0, 3, 0)>(vb), h3 = tr_read<v_rd_off(D0, 3, 1)>(vb);
;   asm volatile("s_waitcnt lgkmcnt(0)" ::: "memory"); SBAR();
;     ...
;   __builtin_amdgcn_s_setprio(1);
;   od = __builtin_amdgcn_mfma_f32_32x32x16_bf16(pa0, PK(l0, h0), od, 0, 0, 0);
;   od = __builtin_amdgcn_mfma_f32_32x32x16_bf16(pa1, PK(l1, h1), od, 0, 0, 0);
;   od = __builtin_amdgcn_mfma_f32_32x32x16_bf16(pa2, PK(l2, h2), od, 0, 0, 0);
;   od = __builtin_amdgcn_mfma_f32_32x32x16_bf16(pa3, PK(l3, h3), od, 0, 0, 0);
;   __builtin_amdgcn_s_setprio(0);
;     ...
; }
; __device__ __forceinline__ void pv_d0(f32x16* o, int vb, bf16x8 pa0, bf16x8 pa1, bf16x8 pa2, bf16x8 pa3) {
;   pv_one<0>(o[0], vb, pa0, pa1, pa2, pa3); pv_one<1>(o[1], vb, pa0, pa1, pa2, pa3);
; __device__ __forceinline__ void attn_body(const bf16_t* __restrict__ Qb, const bf16_t* __restrict__ Kh, const bf16_t* __restrict__ Vh, unsigned char* __restrict__ Ob, int ldo, int seq, LAS char* lds, const int wv, const float kbound, const float oscale) {
;     ...
;     SBAR(); qkt(pB0, pB1, K_lds + b1 * SHM_K, qr, r32, hi, nm);
;     finishSM(pA0, pA1, l_reg, pa0, pa1, pa2, pa3); SBAR();
;     if (j + 3 < NT) SLOAD((j + 3) * KVBLK); SBAR();
;     pv_d0(o, vb0 + b0 * (int)SHM_V, pa0, pa1, pa2, pa3); partialSM(pB0, pB1);
;     __syncthreads();
;     if (j + 3 < NT) SWRITE(b0);
;     SBAR(); if (j + 2 < NT) qkt(pA0, pA1, K_lds + b2 * SHM_K, qr, r32, hi, nm);
;     finishSM(pB0, pB1, l_reg, pa0, pa1, pa2, pa3); SBAR();
;     if (j + 4 < NT) SLOAD((j + 4) * KVBLK); SBAR();
.LBB0_605:
	v_add_u32_e32 v238, v242, v198
	ds_read_b128 v[234:237], v238 offset:24576
	ds_read_b128 v[238:241], v238 offset:32768
	v_add_f32_e32 v33, 0, v80
	v_add_f32_e32 v33, v81, v33
	v_add_f32_e32 v33, v82, v33
	v_add_f32_e32 v33, v83, v33
	v_add_f32_e32 v33, v84, v33
	s_setprio 1
	s_waitcnt lgkmcnt(1)
	v_mfma_f32_32x32x16_bf16 v[112:127], v[234:237], v[128:131], v[48:63]
	v_add_f32_e32 v33, v85, v33
	v_add_f32_e32 v33, v86, v33
	v_add_f32_e32 v33, v87, v33
	v_add_f32_e32 v33, v88, v33
	s_waitcnt lgkmcnt(0)
	v_mfma_f32_32x32x16_bf16 v[96:111], v[238:241], v[128:131], v[48:63]
	s_setprio 0
	v_add_f32_e32 v33, v89, v33
	v_add_f32_e32 v33, v90, v33
	v_add_f32_e32 v33, v91, v33
	v_add_u32_e32 v238, v242, v199
	ds_read_b128 v[234:237], v238 offset:24576
	ds_read_b128 v[238:241], v238 offset:32768
	v_exp_f32_e32 v64, v64
	v_add_f32_e32 v33, v92, v33
	v_exp_f32_e32 v65, v65
	v_add_f32_e32 v33, v93, v33
	v_exp_f32_e32 v66, v66
	s_setprio 1
	s_waitcnt lgkmcnt(1)
	v_mfma_f32_32x32x16_bf16 v[112:127], v[234:237], v[132:135], v[112:127]
	v_add_f32_e32 v33, v94, v33
	v_exp_f32_e32 v67, v67
	v_add_f32_e32 v33, v95, v33
	v_exp_f32_e32 v68, v68
	s_waitcnt lgkmcnt(0)
	v_mfma_f32_32x32x16_bf16 v[96:111], v[238:241], v[132:135], v[96:111]
	s_setprio 0
	v_add_f32_e32 v33, v64, v33
	v_exp_f32_e32 v69, v69
	v_add_f32_e32 v33, v65, v33
	v_add_u32_e32 v238, v242, v200
	ds_read_b128 v[234:237], v238 offset:24576
	ds_read_b128 v[238:241], v238 offset:32768
	v_exp_f32_e32 v70, v70
	v_add_f32_e32 v33, v66, v33
	v_exp_f32_e32 v71, v71
	v_add_f32_e32 v33, v67, v33
	v_exp_f32_e32 v72, v72
	s_setprio 1
	s_waitcnt lgkmcnt(1)
	v_mfma_f32_32x32x16_bf16 v[112:127], v[234:237], v[136:139], v[112:127]
	v_add_f32_e32 v33, v68, v33
	v_exp_f32_e32 v73, v73
	v_add_f32_e32 v33, v69, v33
	v_exp_f32_e32 v74, v74
	s_waitcnt lgkmcnt(0)
	v_mfma_f32_32x32x16_bf16 v[96:111], v[238:241], v[136:139], v[96:111]
	s_setprio 0
	v_add_f32_e32 v33, v70, v33
	v_exp_f32_e32 v75, v75
	v_add_f32_e32 v33, v71, v33
	v_add_u32_e32 v238, v242, v201
	ds_read_b128 v[234:237], v238 offset:24576
	ds_read_b128 v[238:241], v238 offset:32768
	v_exp_f32_e32 v76, v76
	v_add_f32_e32 v33, v72, v33
	v_exp_f32_e32 v77, v77
	v_add_f32_e32 v33, v73, v33
	v_exp_f32_e32 v78, v78
	s_setprio 1
	s_waitcnt lgkmcnt(1)
	v_mfma_f32_32x32x16_bf16 v[112:127], v[234:237], v[140:143], v[112:127]
	v_add_f32_e32 v33, v74, v33
	v_exp_f32_e32 v79, v79
	v_add_f32_e32 v33, v75, v33
	v_add_f32_e32 v33, v76, v33
	s_waitcnt lgkmcnt(0)
	v_mfma_f32_32x32x16_bf16 v[96:111], v[238:241], v[140:143], v[96:111]
	s_setprio 0
	v_add_f32_e32 v33, v77, v33
	v_add_f32_e32 v33, v78, v33
	v_add_f32_e32 v204, v79, v33
	v_add_u32_e32 v238, v242, v202
	ds_read_b128 v[234:237], v238 offset:24576
	ds_read_b128 v[238:241], v238 offset:32768
	v_mov_b32_e32 v205, v204
	v_cvt_pk_bf16_f32 v34, v80, v81
	v_cvt_pk_bf16_f32 v35, v82, v83
	v_cvt_pk_bf16_f32 v36, v84, v85
	v_cvt_pk_bf16_f32 v37, v86, v87
	s_setprio 1
	s_waitcnt lgkmcnt(1)
	v_mfma_f32_32x32x16_bf16 v[112:127], v[234:237], v[148:151], v[112:127]
	v_cvt_pk_bf16_f32 v38, v88, v89
	v_cvt_pk_bf16_f32 v39, v90, v91
	v_cvt_pk_bf16_f32 v40, v92, v93
	v_cvt_pk_bf16_f32 v41, v94, v95
	s_waitcnt lgkmcnt(0)
	v_mfma_f32_32x32x16_bf16 v[96:111], v[238:241], v[148:151], v[96:111]
	s_setprio 0
	v_cvt_pk_bf16_f32 v42, v64, v65
	v_cvt_pk_bf16_f32 v43, v66, v67
	v_cvt_pk_bf16_f32 v44, v68, v69
	v_add_u32_e32 v242, v242, v203
	ds_read_b128 v[234:237], v242 offset:24576
	ds_read_b128 v[238:241], v242 offset:32768
	v_cvt_pk_bf16_f32 v45, v70, v71
	v_cvt_pk_bf16_f32 v164, v72, v73
	v_cvt_pk_bf16_f32 v165, v74, v75
	v_cvt_pk_bf16_f32 v166, v76, v77
	v_cvt_pk_bf16_f32 v167, v78, v79
	s_setprio 1
	s_waitcnt lgkmcnt(1)
	v_mfma_f32_32x32x16_bf16 v[112:127], v[234:237], v[144:147], v[112:127]
	s_nop 1
	v_permlane32_swap_b32_e32 v204, v205
	v_permlane32_swap_b32_e32 v34, v36
	v_permlane32_swap_b32_e32 v35, v37
	s_waitcnt lgkmcnt(0)
	v_mfma_f32_32x32x16_bf16 v[96:111], v[238:241], v[144:147], v[96:111]
	s_setprio 0
	v_permlane32_swap_b32_e32 v38, v40
	v_permlane32_swap_b32_e32 v39, v41
	v_permlane32_swap_b32_e32 v42, v44
	v_permlane32_swap_b32_e32 v43, v45
	v_permlane32_swap_b32_e32 v164, v166
	v_permlane32_swap_b32_e32 v165, v167
	s_lshl_b32 s14, s6, 13
	v_add_u32_e32 v33, s14, v188
	ds_read_b64_tr_b16 v[206:207], v33 offset:0
	ds_read_b64_tr_b16 v[208:209], v33 offset:0x400
	ds_read_b64_tr_b16 v[210:211], v33 offset:0x800
	ds_read_b64_tr_b16 v[212:213], v33 offset:0xc00
	ds_read_b64_tr_b16 v[214:215], v33 offset:0x1000
	ds_read_b64_tr_b16 v[216:217], v33 offset:0x1400
	ds_read_b64_tr_b16 v[218:219], v33 offset:0x1800
	ds_read_b64_tr_b16 v[220:221], v33 offset:0x1c00
	s_waitcnt lgkmcnt(0)
	s_setprio 1
	v_mfma_f32_32x32x16_bf16 v[0:15], v[34:37], v[206:209], v[0:15]
	v_mfma_f32_32x32x16_bf16 v[0:15], v[38:41], v[210:213], v[0:15]
	v_mfma_f32_32x32x16_bf16 v[0:15], v[42:45], v[214:217], v[0:15]
	v_mfma_f32_32x32x16_bf16 v[0:15], v[164:167], v[218:221], v[0:15]
	s_setprio 0
	ds_read_b64_tr_b16 v[206:207], v33 offset:0x200
	ds_read_b64_tr_b16 v[208:209], v33 offset:0x600
	ds_read_b64_tr_b16 v[210:211], v33 offset:0xa00
	ds_read_b64_tr_b16 v[212:213], v33 offset:0xe00
	ds_read_b64_tr_b16 v[214:215], v33 offset:0x1200
	ds_read_b64_tr_b16 v[216:217], v33 offset:0x1600
	ds_read_b64_tr_b16 v[218:219], v33 offset:0x1a00
	ds_read_b64_tr_b16 v[220:221], v33 offset:0x1e00
	s_waitcnt lgkmcnt(0)
	s_setprio 1
	v_mfma_f32_32x32x16_bf16 v[16:31], v[34:37], v[206:209], v[16:31]
	v_mfma_f32_32x32x16_bf16 v[16:31], v[38:41], v[210:213], v[16:31]
	v_mfma_f32_32x32x16_bf16 v[16:31], v[42:45], v[214:217], v[16:31]
	v_mfma_f32_32x32x16_bf16 v[16:31], v[164:167], v[218:221], v[16:31]
	s_setprio 0
	s_andn2_b64 vcc, exec, s[4:5]
	s_barrier
	s_cbranch_vccnz .LBB0_607
	s_lshl_b32 s4, s6, 14
	s_add_i32 s4, s4, 0
	v_add_u32_e32 v35, s14, v189
	v_add_u32_e32 v33, s4, v191
	v_add_u32_e32 v34, s4, v190
	s_waitcnt vmcnt(2)
	ds_write_b128 v35, v[152:155]
	s_waitcnt vmcnt(1)
	ds_write_b128 v34, v[156:159] offset:24576
	s_waitcnt vmcnt(0)
	ds_write_b128 v33, v[160:163] offset:24576
.LBB0_607:
	s_cmp_lt_u32 s71, 60
	s_cselect_b64 s[16:17], -1, 0
	s_cmp_gt_u32 s71, 59
	s_cbranch_scc1 .LBB0_611
	s_waitcnt lgkmcnt(0)
	v_add_co_u32_e32 v252, vcc, 0x66008000, v180
	s_nop 1
	v_addc_co_u32_e32 v253, vcc, 0, v181, vcc
	v_add_co_u32_e32 v254, vcc, 0x62010000, v178
	s_nop 1
	v_addc_co_u32_e32 v255, vcc, 0, v179, vcc
	global_load_dwordx4 v[152:155], v[252:253], off
	global_load_dwordx4 v[156:159], v[254:255], off
	v_add_co_u32_e32 v252, vcc, 0x62012000, v178
	s_nop 1
	v_addc_co_u32_e32 v253, vcc, 0, v179, vcc
	global_load_dwordx4 v[160:163], v[252:253], off

; #define LAS __attribute__((address_space(3)))
; #define SBAR() __builtin_amdgcn_sched_barrier(0)
; #define SLOAD(k0) do { sr_.vs0 = *reinterpret_cast<const bf16x8*>(&Vh[(long)((k0) + vr) * DVV + vc]); \
;     sr_.ks0 = *reinterpret_cast<const bf16x8*>(&Kh[(long)((k0) + sr) * KROW + sc]); sr_.ks1 = *reinterpret_cast<const bf16x8*>(&Kh[(long)((k0) + 32 + sr) * KROW + sc]); } while (0)
; __device__ __forceinline__ void qkt(f32x16& p0, f32x16& p1, const LAS char* Ks, const bf16x8* qr, int r32, int hi, float nm) {
; #pragma unroll
;   for (int r = 0; r < 16; ++r) { p0[r] = nm; p1[r] = nm; }
; #pragma unroll
;   for (int d0 = 0; d0 < DQK / 16; ++d0) { int cb = (d0 * 16 + hi * 8) * 2;
;     bf16x8 b0 = *reinterpret_cast<const LAS bf16x8*>(Ks + KSWZ(r32, cb));
;     bf16x8 b1 = *reinterpret_cast<const LAS bf16x8*>(Ks + KSWZ(32 + r32, cb));
;     __builtin_amdgcn_s_setprio(1);
;     p0 = __builtin_amdgcn_mfma_f32_32x32x16_bf16(b0, qr[d0], p0, 0, 0, 0);
;     p1 = __builtin_amdgcn_mfma_f32_32x32x16_bf16(b1, qr[d0], p1, 0, 0, 0);
;     __builtin_amdgcn_s_setprio(0); }
; }
; __device__ __forceinline__ void attn_body(const bf16_t* __restrict__ Qb, const bf16_t* __restrict__ Kh, const bf16_t* __restrict__ Vh, unsigned char* __restrict__ Ob, int ldo, int seq, LAS char* lds, const int wv, const float kbound, const float oscale) {
;     ...
;     SBAR(); qkt(pB0, pB1, K_lds + b1 * SHM_K, qr, r32, hi, nm);
;     finishSM(pA0, pA1, l_reg, pa0, pa1, pa2, pa3); SBAR();
;     if (j + 3 < NT) SLOAD((j + 3) * KVBLK); SBAR();
.LBB0_3144:
	s_mov_b32 s74, s4
	s_lshl_b32 s4, s72, 14
	s_add_i32 s75, s4, 0
	v_add_u32_e32 v242, s75, v192
	s_cmp_lt_u32 s73, 61
	s_cselect_b64 s[4:5], -1, 0
	s_cmp_gt_u32 s73, 60
	v_lshl_add_u64 v[180:181], s[22:23], 0, v[176:177]
	v_lshl_add_u64 v[178:179], s[22:23], 0, v[174:175]
	s_cbranch_scc1 .LBB0_3146
	s_waitcnt lgkmcnt(0)
	v_add_co_u32_e32 v46, vcc, 0x66006000, v180
	s_nop 1
	v_addc_co_u32_e32 v47, vcc, 0, v181, vcc
	s_waitcnt vmcnt(1)
	v_add_co_u32_e32 v156, vcc, 0x6200c000, v178
	s_nop 1
	v_addc_co_u32_e32 v157, vcc, 0, v179, vcc
	global_load_dwordx4 v[152:155], v[46:47], off
	s_nop 0
	global_load_dwordx4 v[156:159], v[156:157], off
	v_add_co_u32_e32 v46, vcc, 0x6200e000, v178
	s_nop 1
	v_addc_co_u32_e32 v47, vcc, 0, v179, vcc
	global_load_dwordx4 v[160:163], v[46:47], off

; #define SBAR() __builtin_amdgcn_sched_barrier(0)
; #define SLOAD(k0) do { sr_.vs0 = *reinterpret_cast<const bf16x8*>(&Vh[(long)((k0) + vr) * DVV + vc]); \
;     sr_.ks0 = *reinterpret_cast<const bf16x8*>(&Kh[(long)((k0) + sr) * KROW + sc]); sr_.ks1 = *reinterpret_cast<const bf16x8*>(&Kh[(long)((k0) + 32 + sr) * KROW + sc]); } while (0)
; __device__ __forceinline__ void attn_body(const bf16_t* __restrict__ Qb, const bf16_t* __restrict__ Kh, const bf16_t* __restrict__ Vh, unsigned char* __restrict__ Ob, int ldo, int seq, LAS char* lds, const int wv, const float kbound, const float oscale) {
;     ...
;     if (j + 4 < NT) SLOAD((j + 4) * KVBLK); SBAR();
.LBB0_3148:
	s_cmp_lt_u32 s73, 60
	s_cselect_b64 s[16:17], -1, 0
	s_cmp_gt_u32 s73, 59
	s_cbranch_scc1 .LBB0_3152
	s_waitcnt lgkmcnt(0)
	v_add_co_u32_e32 v252, vcc, 0x66008000, v180
	s_nop 1
	v_addc_co_u32_e32 v253, vcc, 0, v181, vcc
	v_add_co_u32_e32 v254, vcc, 0x62010000, v178
	s_nop 1
	v_addc_co_u32_e32 v255, vcc, 0, v179, vcc
	global_load_dwordx4 v[152:155], v[252:253], off
	global_load_dwordx4 v[156:159], v[254:255], off
	v_add_co_u32_e32 v252, vcc, 0x62012000, v178
	s_nop 1
	v_addc_co_u32_e32 v253, vcc, 0, v179, vcc
	global_load_dwordx4 v[160:163], v[252:253], off
